# zero accumulators with v_mov_b64 pairs instead of 128 v_mov_b32 per GEMM unit
# speedup vs baseline: 1.0142x; 1.0142x over previous
; template <class Epi, class Sched, bool ALIGN_EPI = false, bool SP2 = false, bool F8 = false>
; __device__ __forceinline__ void gemm_phase(PG8_LAS unsigned char* lds, const Gemm g, const Sched& S, const Epi& E) {
;     ...
;         const bool has_next = S.next(ui + 1, nxt);
;         const char* nA = has_next ? (const char*)g.A + (size_t)nxt.pm * tstep + nxt.ko : cA; const char* nB = has_next ? (const char*)g.Bt + (size_t)nxt.pn * tstep + nxt.ko : cB;
;     ...
; #pragma unroll
;         for (int a = 0; a < 2; ++a)
; #pragma unroll
;             for (int b = 0; b < 2; ++b)
; #pragma unroll
;                 for (int m = 0; m < 4; ++m)
; #pragma unroll
;                     for (int n = 0; n < 2; ++n) acc[a][b][m][n] = (f32x4){0.f, 0.f, 0.f, 0.f};
;         cur = nxt; cA = nA; cB = nB; ++ui;
.LBB0_150:
	s_ashr_i32 s25, s24, 31
	s_lshl_b64 s[4:5], s[24:25], 18
	s_add_u32 s38, s77, s4
	s_addc_u32 s39, s78, s5
	s_and_b64 s[4:5], s[8:9], exec
	s_cselect_b32 s25, s39, s71
	s_cselect_b32 s91, s38, s70
	s_ashr_i32 s31, s30, 31
	s_lshl_b64 s[4:5], s[30:31], 18
	s_add_u32 s42, s79, s4
	s_addc_u32 s43, s80, s5
	s_and_b64 s[4:5], s[8:9], exec
	s_cselect_b32 s31, s43, s73
	s_cselect_b32 s92, s42, s72
	s_add_u32 s70, s70, 0x20080
	s_addc_u32 s71, s71, 0
	s_add_u32 s93, s72, 0x100
	v_mov_b32_e32 v34, 0
	s_addc_u32 s95, s73, 0
	s_mov_b32 s96, -2
	v_mov_b32_e32 v35, 0
	v_mov_b64_e32 v[36:37], 0
	v_mov_b64_e32 v[38:39], 0
	v_mov_b64_e32 v[40:41], 0
	v_mov_b64_e32 v[42:43], 0
	v_mov_b64_e32 v[44:45], 0
	v_mov_b64_e32 v[46:47], 0
	v_mov_b64_e32 v[48:49], 0
	v_mov_b64_e32 v[50:51], 0
	v_mov_b64_e32 v[52:53], 0
	v_mov_b64_e32 v[54:55], 0
	v_mov_b64_e32 v[56:57], 0
	v_mov_b64_e32 v[58:59], 0
	v_mov_b64_e32 v[60:61], 0
	v_mov_b64_e32 v[62:63], 0
	v_mov_b64_e32 v[64:65], 0
	v_mov_b64_e32 v[66:67], 0
	v_mov_b64_e32 v[68:69], 0
	v_mov_b64_e32 v[70:71], 0
	v_mov_b64_e32 v[72:73], 0
	v_mov_b64_e32 v[74:75], 0
	v_mov_b64_e32 v[76:77], 0
	v_mov_b64_e32 v[78:79], 0
	v_mov_b64_e32 v[80:81], 0
	v_mov_b64_e32 v[82:83], 0
	v_mov_b64_e32 v[84:85], 0
	v_mov_b64_e32 v[86:87], 0
	v_mov_b64_e32 v[88:89], 0
	v_mov_b64_e32 v[90:91], 0
	v_mov_b64_e32 v[92:93], 0
	v_mov_b64_e32 v[94:95], 0
	v_mov_b64_e32 v[96:97], 0
	v_mov_b64_e32 v[98:99], 0
	v_mov_b64_e32 v[100:101], 0
	v_mov_b64_e32 v[102:103], 0
	v_mov_b64_e32 v[104:105], 0
	v_mov_b64_e32 v[106:107], 0
	v_mov_b64_e32 v[108:109], 0
	v_mov_b64_e32 v[110:111], 0
	v_mov_b64_e32 v[112:113], 0
	v_mov_b64_e32 v[114:115], 0
	v_mov_b64_e32 v[116:117], 0
	v_mov_b64_e32 v[118:119], 0
	v_mov_b64_e32 v[120:121], 0
	v_mov_b64_e32 v[122:123], 0
	v_mov_b64_e32 v[124:125], 0
	v_mov_b64_e32 v[126:127], 0
	v_mov_b64_e32 v[128:129], 0
	v_mov_b64_e32 v[130:131], 0
	v_mov_b64_e32 v[132:133], 0
	v_mov_b64_e32 v[134:135], 0
	v_mov_b64_e32 v[136:137], 0
	v_mov_b64_e32 v[138:139], 0
	v_mov_b64_e32 v[140:141], 0
	v_mov_b64_e32 v[142:143], 0
	v_mov_b64_e32 v[144:145], 0
	v_mov_b64_e32 v[146:147], 0
	v_mov_b64_e32 v[148:149], 0
	v_mov_b64_e32 v[150:151], 0
	v_mov_b64_e32 v[152:153], 0
	v_mov_b64_e32 v[154:155], 0
	v_mov_b64_e32 v[156:157], 0
	v_mov_b64_e32 v[158:159], 0
	v_mov_b64_e32 v[160:161], 0

; template <class Epi, class Sched, bool ALIGN_EPI = false, bool SP2 = false, bool F8 = false>
; __device__ __forceinline__ void gemm_phase(PG8_LAS unsigned char* lds, const Gemm g, const Sched& S, const Epi& E) {
;     ...
;     const int tid = tid_, wid = __builtin_amdgcn_readfirstlane(tid >> 6), lane = tid & 63, wr = wid >> 2, wc = wid & 3, fr = lane & 15, fq = lane >> 4;
;     const int K = g.K, nt = g.nt ? g.nt : K / BK;
;     unsigned voffA[2], voffB[2];
; #pragma unroll
;     for (int i = 0; i < 2; ++i) { int R, C; stage_rc(tid * 16 + i * 8192, R, C); const int Rb = Epi::PERM ? ((R & ~31) + perm32(R & 31)) : R;
;         voffA[i] = (unsigned)(R * K + C) * 2u; voffB[i] = (unsigned)(Rb * K + C) * 2u; }
;     const size_t kstep = (size_t)(BK * 2);
;     const size_t hstep = (size_t)HALF * K * 2;
;     const size_t tstep = 2 * hstep;
;     const unsigned ldsw = (unsigned)wid * 1024u;
;     const int aoff = lds_byte(wr * 64 + fr, fq * 8), boff = lds_byte(wc * 32 + fr, fq * 8);
;     ...
;     Unit cur, nxt; int ui = 0;
;     if (!S.next(0, cur)) return;
;     f32x4 acc[2][2][4][2];
;     if constexpr (Epi::INIT_ACC) E.init(acc, cur, wr, wc, fr, fq);
;     else {
; #pragma unroll
;     for (int a = 0; a < 2; ++a)
; #pragma unroll
;         for (int b = 0; b < 2; ++b)
; #pragma unroll
;             for (int m = 0; m < 4; ++m)
; #pragma unroll
;                 for (int n = 0; n < 2; ++n) acc[a][b][m][n] = (f32x4){0.f, 0.f, 0.f, 0.f};
;     }
;     typename Frag<F8>::A At[4]; typename Frag<F8>::A B0[2], B1[2];
;     const char* cA = (const char*)g.A + (size_t)cur.pm * tstep + cur.ko; const char* cB = (const char*)g.Bt + (size_t)cur.pn * tstep + cur.ko;
;     S.a_ready(cur);
;     if constexpr (SP2) {
;         PG8_STAGE(PG8_SB(0, 0), cB, voffB); PG8_STAGE(PG8_SB(0, 1), cB + hstep, voffB); PG8_STAGE(PG8_SA(0, 0), cA, voffA); PG8_STAGE(PG8_SA(0, 1), cA + hstep, voffA);
;         if (wr == 1) PG8_BAR;
;         PG8_WAIT_V(2); PG8_BAR;
;         PG8_STAGE(PG8_SB(1, 0), cB + kstep, voffB); PG8_STAGE(PG8_SA(1, 0), cA + kstep, voffA); PG8_STAGE(PG8_SB(1, 1), cB + hstep + kstep, voffB);
;         PG8_WAIT_V(6); PG8_BAR;
;     } else {
;         PG8_STAGE(PG8_SB(0, 0), cB, voffB); PG8_STAGE(PG8_SA(0, 0), cA, voffA); PG8_STAGE(PG8_SB(0, 1), cB + hstep, voffB); PG8_STAGE(PG8_SA(0, 1), cA + hstep, voffA);
;         if (wr == 1) PG8_BAR;
;         PG8_WAIT_V(4); PG8_BAR;
.LBB0_161:
	v_lshrrev_b32_e32 v14, 1, v9
	v_and_b32_e32 v165, 24, v14
	v_and_b32_e32 v13, 15, v9
	v_lshlrev_b32_e32 v14, 1, v165
	v_lshlrev_b32_e32 v9, 2, v9
	v_lshl_or_b32 v166, s5, 6, v13
	v_lshl_or_b32 v13, v13, 6, v14
	s_lshl_b32 s0, s5, 13
	v_and_b32_e32 v9, 32, v9
	v_bitop3_b32 v14, v13, s0, v9 bitop3:0xde
	s_lshl_b32 s0, s4, 5
	s_mov_b64 s[14:15], 0x80
	s_and_b32 s42, s0, 0x60
	s_add_i32 m0, s30, 0x18000
	v_lshl_add_u64 v[4:5], v[4:5], 0, s[14:15]
	s_lshl_b32 s0, s42, 7
	s_waitcnt vmcnt(2)
	s_barrier
	global_load_lds_dwordx4 v[4:5], off
	s_add_i32 m0, s30, 0x1a000
	s_add_u32 s4, s34, 0x100080
	v_lshl_add_u64 v[2:3], v[2:3], 0, s[14:15]
	s_addc_u32 s5, s35, 0
	s_add_i32 s43, s30, 0x8000
	global_load_lds_dwordx4 v[2:3], off
	v_lshl_add_u64 v[2:3], s[4:5], 0, v[174:175]
	s_mov_b32 m0, s43
	s_add_i32 s44, s30, 0xa000
	global_load_lds_dwordx4 v[2:3], off
	v_lshl_add_u64 v[2:3], s[4:5], 0, v[170:171]
	s_add_u32 s4, s12, 0x20080
	s_mov_b32 m0, s44
	s_addc_u32 s5, s13, 0
	global_load_lds_dwordx4 v[2:3], off
	s_add_i32 m0, s30, 0x1c000
	v_lshl_add_u64 v[2:3], s[4:5], 0, v[172:173]
	global_load_lds_dwordx4 v[2:3], off
	v_lshl_add_u64 v[2:3], s[4:5], 0, v[168:169]
	s_add_i32 m0, s30, 0x1e000
	s_mov_b64 s[4:5], 0x120080
	global_load_lds_dwordx4 v[2:3], off
	v_lshlrev_b32_e32 v2, 13, v11
	v_and_b32_e32 v2, 0xffffc000, v2
	v_lshl_add_u32 v2, v10, 10, v2
	v_and_b32_e32 v3, 1, v11
	v_lshl_or_b32 v2, v3, 6, v2
	v_lshl_add_u32 v2, v12, 1, v2
	v_mov_b32_e32 v3, v173
	v_lshl_add_u64 v[176:177], v[2:3], 0, s[4:5]
	v_lshlrev_b32_e32 v2, 13, v6
	v_and_b32_e32 v2, 0xffffc000, v2
	v_lshl_add_u32 v2, v7, 10, v2
	v_and_b32_e32 v3, 1, v6
	s_add_u32 s45, s6, 0x700100
	v_bitop3_b32 v9, v13, s0, v9 bitop3:0xde
	s_waitcnt vmcnt(6)
	v_lshl_or_b32 v2, v3, 6, v2
	s_addc_u32 s70, 0, 0
	s_add_i32 s74, 0, 0x10000
	s_add_i32 s76, 0, 0x14000
	s_add_i32 s78, 0, 0x18000
	s_add_i32 s80, 0, 0x1c000
	v_lshl_add_u32 v2, v8, 1, v2
	v_mov_b32_e32 v3, v173
	v_add_u32_e32 v167, s74, v9
	v_add_u32_e32 v188, s76, v9
	s_add_i32 s74, s74, s3
	s_add_i32 s76, s76, s3
	v_add_u32_e32 v191, s78, v9
	v_add_u32_e32 v192, s80, v9
	s_add_i32 s78, s78, s3
	s_add_i32 s80, s80, s3
	v_lshl_add_u64 v[178:179], v[2:3], 0, s[4:5]
	s_mov_b32 s71, -2
	v_add_u32_e32 v189, 0, v14
	s_add_i32 s72, s30, 0xc000
	s_add_i32 s73, s30, 0xe000
	v_mov_b32_e32 v190, 0x7f7f7f7f
	s_add_i32 s75, s74, 0x2000
	s_add_i32 s77, s76, 0x2000
	s_add_i32 s79, s78, 0x2000
	s_add_i32 s81, s80, 0x2000
	s_mov_b64 s[16:17], s[34:35]
	v_mov_b64_e32 v[34:35], 0
	v_mov_b64_e32 v[36:37], 0
	v_mov_b64_e32 v[38:39], 0
	v_mov_b64_e32 v[40:41], 0
	v_mov_b64_e32 v[42:43], 0
	v_mov_b64_e32 v[44:45], 0
	v_mov_b64_e32 v[46:47], 0
	v_mov_b64_e32 v[48:49], 0
	v_mov_b64_e32 v[50:51], 0
	v_mov_b64_e32 v[52:53], 0
	v_mov_b64_e32 v[54:55], 0
	v_mov_b64_e32 v[56:57], 0
	v_mov_b64_e32 v[58:59], 0
	v_mov_b64_e32 v[60:61], 0
	v_mov_b64_e32 v[62:63], 0
	v_mov_b64_e32 v[64:65], 0
	v_mov_b64_e32 v[66:67], 0
	v_mov_b64_e32 v[68:69], 0
	v_mov_b64_e32 v[70:71], 0
	v_mov_b64_e32 v[72:73], 0
	v_mov_b64_e32 v[74:75], 0
	v_mov_b64_e32 v[76:77], 0
	v_mov_b64_e32 v[78:79], 0
	v_mov_b64_e32 v[80:81], 0
	v_mov_b64_e32 v[82:83], 0
	v_mov_b64_e32 v[84:85], 0
	v_mov_b64_e32 v[86:87], 0
	v_mov_b64_e32 v[88:89], 0
	v_mov_b64_e32 v[90:91], 0
	v_mov_b64_e32 v[92:93], 0
	v_mov_b64_e32 v[94:95], 0
	v_mov_b64_e32 v[96:97], 0
	v_mov_b64_e32 v[98:99], 0
	v_mov_b64_e32 v[100:101], 0
	v_mov_b64_e32 v[102:103], 0
	v_mov_b64_e32 v[104:105], 0
	v_mov_b64_e32 v[106:107], 0
	v_mov_b64_e32 v[108:109], 0
	v_mov_b64_e32 v[110:111], 0
	v_mov_b64_e32 v[112:113], 0
	v_mov_b64_e32 v[114:115], 0
	v_mov_b64_e32 v[116:117], 0
	v_mov_b64_e32 v[118:119], 0
	v_mov_b64_e32 v[120:121], 0
	v_mov_b64_e32 v[122:123], 0
	v_mov_b64_e32 v[124:125], 0
	v_mov_b64_e32 v[126:127], 0
	v_mov_b64_e32 v[128:129], 0
	v_mov_b64_e32 v[130:131], 0
	v_mov_b64_e32 v[132:133], 0
	v_mov_b64_e32 v[134:135], 0
	v_mov_b64_e32 v[136:137], 0
	v_mov_b64_e32 v[138:139], 0
	v_mov_b64_e32 v[140:141], 0
	v_mov_b64_e32 v[142:143], 0
	v_mov_b64_e32 v[144:145], 0
	v_mov_b64_e32 v[146:147], 0
	v_mov_b64_e32 v[148:149], 0
	v_mov_b64_e32 v[150:151], 0
	v_mov_b64_e32 v[152:153], 0
	v_mov_b64_e32 v[154:155], 0
	v_mov_b64_e32 v[156:157], 0
	v_mov_b64_e32 v[158:159], 0
	v_mov_b64_e32 v[160:161], 0
	s_barrier

; template <class Epi, class Sched, bool ALIGN_EPI = false, bool SP2 = false, bool F8 = false>
; __device__ __forceinline__ void gemm_phase(PG8_LAS unsigned char* lds, const Gemm g, const Sched& S, const Epi& E) {
;     ...
;     const int tid = tid_, wid = __builtin_amdgcn_readfirstlane(tid >> 6), lane = tid & 63, wr = wid >> 2, wc = wid & 3, fr = lane & 15, fq = lane >> 4;
;     const int K = g.K, nt = g.nt ? g.nt : K / BK;
;     unsigned voffA[2], voffB[2];
; #pragma unroll
;     for (int i = 0; i < 2; ++i) { int R, C; stage_rc(tid * 16 + i * 8192, R, C); const int Rb = Epi::PERM ? ((R & ~31) + perm32(R & 31)) : R;
;         voffA[i] = (unsigned)(R * K + C) * 2u; voffB[i] = (unsigned)(Rb * K + C) * 2u; }
;     const size_t kstep = (size_t)(BK * 2);
;     const size_t hstep = (size_t)HALF * K * 2;
;     const size_t tstep = 2 * hstep;
;     const unsigned ldsw = (unsigned)wid * 1024u;
;     const int aoff = lds_byte(wr * 64 + fr, fq * 8), boff = lds_byte(wc * 32 + fr, fq * 8);
;     ...
;     Unit cur, nxt; int ui = 0;
;     if (!S.next(0, cur)) return;
;     f32x4 acc[2][2][4][2];
;     if constexpr (Epi::INIT_ACC) E.init(acc, cur, wr, wc, fr, fq);
;     else {
; #pragma unroll
;     for (int a = 0; a < 2; ++a)
; #pragma unroll
;         for (int b = 0; b < 2; ++b)
; #pragma unroll
;             for (int m = 0; m < 4; ++m)
; #pragma unroll
;                 for (int n = 0; n < 2; ++n) acc[a][b][m][n] = (f32x4){0.f, 0.f, 0.f, 0.f};
;     }
;     typename Frag<F8>::A At[4]; typename Frag<F8>::A B0[2], B1[2];
;     const char* cA = (const char*)g.A + (size_t)cur.pm * tstep + cur.ko; const char* cB = (const char*)g.Bt + (size_t)cur.pn * tstep + cur.ko;
;     S.a_ready(cur);
;     if constexpr (SP2) {
;         PG8_STAGE(PG8_SB(0, 0), cB, voffB); PG8_STAGE(PG8_SB(0, 1), cB + hstep, voffB); PG8_STAGE(PG8_SA(0, 0), cA, voffA); PG8_STAGE(PG8_SA(0, 1), cA + hstep, voffA);
;         if (wr == 1) PG8_BAR;
;         PG8_WAIT_V(2); PG8_BAR;
;         PG8_STAGE(PG8_SB(1, 0), cB + kstep, voffB); PG8_STAGE(PG8_SA(1, 0), cA + kstep, voffA); PG8_STAGE(PG8_SB(1, 1), cB + hstep + kstep, voffB);
;         PG8_WAIT_V(6); PG8_BAR;
;     } else {
;         PG8_STAGE(PG8_SB(0, 0), cB, voffB); PG8_STAGE(PG8_SA(0, 0), cA, voffA); PG8_STAGE(PG8_SB(0, 1), cB + hstep, voffB); PG8_STAGE(PG8_SA(0, 1), cA + hstep, voffA);
;         if (wr == 1) PG8_BAR;
;         PG8_WAIT_V(4); PG8_BAR;
.LBB0_169:
	v_lshrrev_b32_e32 v14, 1, v9
	v_and_b32_e32 v165, 24, v14
	v_and_b32_e32 v13, 15, v9
	v_lshlrev_b32_e32 v14, 1, v165
	v_lshlrev_b32_e32 v9, 2, v9
	v_lshl_or_b32 v166, s5, 6, v13
	v_lshl_or_b32 v13, v13, 6, v14
	s_lshl_b32 s0, s5, 13
	v_and_b32_e32 v9, 32, v9
	v_bitop3_b32 v14, v13, s0, v9 bitop3:0xde
	s_lshl_b32 s0, s4, 5
	s_mov_b64 s[14:15], 0x80
	s_and_b32 s42, s0, 0x60
	s_add_i32 m0, s30, 0x18000
	v_lshl_add_u64 v[4:5], v[4:5], 0, s[14:15]
	s_lshl_b32 s0, s42, 7
	s_waitcnt vmcnt(2)
	s_barrier
	global_load_lds_dwordx4 v[4:5], off
	s_add_i32 m0, s30, 0x1a000
	s_add_u32 s4, s34, 0x100080
	v_lshl_add_u64 v[2:3], v[2:3], 0, s[14:15]
	s_addc_u32 s5, s35, 0
	s_add_i32 s43, s30, 0x8000
	global_load_lds_dwordx4 v[2:3], off
	v_lshl_add_u64 v[2:3], s[4:5], 0, v[174:175]
	s_mov_b32 m0, s43
	s_add_i32 s44, s30, 0xa000
	global_load_lds_dwordx4 v[2:3], off
	v_lshl_add_u64 v[2:3], s[4:5], 0, v[170:171]
	s_add_u32 s4, s12, 0x20080
	s_mov_b32 m0, s44
	s_addc_u32 s5, s13, 0
	global_load_lds_dwordx4 v[2:3], off
	s_add_i32 m0, s30, 0x1c000
	v_lshl_add_u64 v[2:3], s[4:5], 0, v[172:173]
	global_load_lds_dwordx4 v[2:3], off
	v_lshl_add_u64 v[2:3], s[4:5], 0, v[168:169]
	s_add_i32 m0, s30, 0x1e000
	s_mov_b64 s[4:5], 0x120080
	global_load_lds_dwordx4 v[2:3], off
	v_lshlrev_b32_e32 v2, 13, v11
	v_and_b32_e32 v2, 0xffffc000, v2
	v_lshl_add_u32 v2, v10, 10, v2
	v_and_b32_e32 v3, 1, v11
	v_lshl_or_b32 v2, v3, 6, v2
	v_lshl_add_u32 v2, v12, 1, v2
	v_mov_b32_e32 v3, v173
	v_lshl_add_u64 v[176:177], v[2:3], 0, s[4:5]
	v_lshlrev_b32_e32 v2, 13, v6
	v_and_b32_e32 v2, 0xffffc000, v2
	v_lshl_add_u32 v2, v7, 10, v2
	v_and_b32_e32 v3, 1, v6
	s_add_u32 s45, s6, 0x800100
	v_bitop3_b32 v9, v13, s0, v9 bitop3:0xde
	s_waitcnt vmcnt(6)
	v_lshl_or_b32 v2, v3, 6, v2
	s_addc_u32 s70, 0, 0
	s_add_i32 s74, 0, 0x10000
	s_add_i32 s76, 0, 0x14000
	s_add_i32 s78, 0, 0x18000
	s_add_i32 s80, 0, 0x1c000
	v_lshl_add_u32 v2, v8, 1, v2
	v_mov_b32_e32 v3, v173
	v_add_u32_e32 v167, s74, v9
	v_add_u32_e32 v188, s76, v9
	s_add_i32 s74, s74, s3
	s_add_i32 s76, s76, s3
	v_add_u32_e32 v191, s78, v9
	v_add_u32_e32 v192, s80, v9
	s_add_i32 s78, s78, s3
	s_add_i32 s80, s80, s3
	v_lshl_add_u64 v[178:179], v[2:3], 0, s[4:5]
	s_mov_b32 s71, -2
	v_add_u32_e32 v189, 0, v14
	s_add_i32 s72, s30, 0xc000
	s_add_i32 s73, s30, 0xe000
	v_mov_b32_e32 v190, 0x7f7f7f7f
	s_add_i32 s75, s74, 0x2000
	s_add_i32 s77, s76, 0x2000
	s_add_i32 s79, s78, 0x2000
	s_add_i32 s81, s80, 0x2000
	s_mov_b64 s[16:17], s[34:35]
	v_mov_b64_e32 v[34:35], 0
	v_mov_b64_e32 v[36:37], 0
	v_mov_b64_e32 v[38:39], 0
	v_mov_b64_e32 v[40:41], 0
	v_mov_b64_e32 v[42:43], 0
	v_mov_b64_e32 v[44:45], 0
	v_mov_b64_e32 v[46:47], 0
	v_mov_b64_e32 v[48:49], 0
	v_mov_b64_e32 v[50:51], 0
	v_mov_b64_e32 v[52:53], 0
	v_mov_b64_e32 v[54:55], 0
	v_mov_b64_e32 v[56:57], 0
	v_mov_b64_e32 v[58:59], 0
	v_mov_b64_e32 v[60:61], 0
	v_mov_b64_e32 v[62:63], 0
	v_mov_b64_e32 v[64:65], 0
	v_mov_b64_e32 v[66:67], 0
	v_mov_b64_e32 v[68:69], 0
	v_mov_b64_e32 v[70:71], 0
	v_mov_b64_e32 v[72:73], 0
	v_mov_b64_e32 v[74:75], 0
	v_mov_b64_e32 v[76:77], 0
	v_mov_b64_e32 v[78:79], 0
	v_mov_b64_e32 v[80:81], 0
	v_mov_b64_e32 v[82:83], 0
	v_mov_b64_e32 v[84:85], 0
	v_mov_b64_e32 v[86:87], 0
	v_mov_b64_e32 v[88:89], 0
	v_mov_b64_e32 v[90:91], 0
	v_mov_b64_e32 v[92:93], 0
	v_mov_b64_e32 v[94:95], 0
	v_mov_b64_e32 v[96:97], 0
	v_mov_b64_e32 v[98:99], 0
	v_mov_b64_e32 v[100:101], 0
	v_mov_b64_e32 v[102:103], 0
	v_mov_b64_e32 v[104:105], 0
	v_mov_b64_e32 v[106:107], 0
	v_mov_b64_e32 v[108:109], 0
	v_mov_b64_e32 v[110:111], 0
	v_mov_b64_e32 v[112:113], 0
	v_mov_b64_e32 v[114:115], 0
	v_mov_b64_e32 v[116:117], 0
	v_mov_b64_e32 v[118:119], 0
	v_mov_b64_e32 v[120:121], 0
	v_mov_b64_e32 v[122:123], 0
	v_mov_b64_e32 v[124:125], 0
	v_mov_b64_e32 v[126:127], 0
	v_mov_b64_e32 v[128:129], 0
	v_mov_b64_e32 v[130:131], 0
	v_mov_b64_e32 v[132:133], 0
	v_mov_b64_e32 v[134:135], 0
	v_mov_b64_e32 v[136:137], 0
	v_mov_b64_e32 v[138:139], 0
	v_mov_b64_e32 v[140:141], 0
	v_mov_b64_e32 v[142:143], 0
	v_mov_b64_e32 v[144:145], 0
	v_mov_b64_e32 v[146:147], 0
	v_mov_b64_e32 v[148:149], 0
	v_mov_b64_e32 v[150:151], 0
	v_mov_b64_e32 v[152:153], 0
	v_mov_b64_e32 v[154:155], 0
	v_mov_b64_e32 v[156:157], 0
	v_mov_b64_e32 v[158:159], 0
	v_mov_b64_e32 v[160:161], 0
	s_barrier

; template <class Epi, class Sched, bool ALIGN_EPI = false, bool SP2 = false, bool F8 = false>
; __device__ __forceinline__ void gemm_phase(PG8_LAS unsigned char* lds, const Gemm g, const Sched& S, const Epi& E) {
;     ...
;         const bool has_next = S.next(ui + 1, nxt);
;         const char* nA = has_next ? (const char*)g.A + (size_t)nxt.pm * tstep + nxt.ko : cA; const char* nB = has_next ? (const char*)g.Bt + (size_t)nxt.pn * tstep + nxt.ko : cB;
;     ...
; #pragma unroll
;         for (int a = 0; a < 2; ++a)
; #pragma unroll
;             for (int b = 0; b < 2; ++b)
; #pragma unroll
;                 for (int m = 0; m < 4; ++m)
; #pragma unroll
;                     for (int n = 0; n < 2; ++n) acc[a][b][m][n] = (f32x4){0.f, 0.f, 0.f, 0.f};
;         cur = nxt; cA = nA; cB = nB; ++ui;
.LBB0_561:
	s_ashr_i32 s25, s24, 31
	s_lshl_b64 s[4:5], s[24:25], 19
	s_add_u32 s36, s50, s4
	s_addc_u32 s37, s51, s5
	s_and_b64 s[4:5], s[8:9], exec
	s_cselect_b32 s6, s37, s43
	s_cselect_b32 s7, s36, s42
	s_ashr_i32 s31, s30, 31
	s_lshl_b64 s[4:5], s[30:31], 19
	s_add_u32 s38, s52, s4
	s_addc_u32 s39, s53, s5
	s_and_b64 s[4:5], s[8:9], exec
	s_cselect_b32 s25, s39, s45
	s_cselect_b32 s31, s38, s44
	s_add_u32 s42, s42, 0x40080
	s_addc_u32 s43, s43, 0
	s_add_u32 s84, s44, 0x100
	v_mov_b32_e32 v2, 0
	s_addc_u32 s85, s45, 0
	s_mov_b32 s86, -2
	v_mov_b32_e32 v3, 0
	v_mov_b64_e32 v[4:5], 0
	v_mov_b64_e32 v[6:7], 0
	v_mov_b64_e32 v[8:9], 0
	v_mov_b64_e32 v[10:11], 0
	v_mov_b64_e32 v[12:13], 0
	v_mov_b64_e32 v[14:15], 0
	v_mov_b64_e32 v[16:17], 0
	v_mov_b64_e32 v[18:19], 0
	v_mov_b64_e32 v[20:21], 0
	v_mov_b64_e32 v[22:23], 0
	v_mov_b64_e32 v[24:25], 0
	v_mov_b64_e32 v[26:27], 0
	v_mov_b64_e32 v[28:29], 0
	v_mov_b64_e32 v[30:31], 0
	v_mov_b64_e32 v[32:33], 0
	v_mov_b64_e32 v[34:35], 0
	v_mov_b64_e32 v[36:37], 0
	v_mov_b64_e32 v[38:39], 0
	v_mov_b64_e32 v[40:41], 0
	v_mov_b64_e32 v[42:43], 0
	v_mov_b64_e32 v[44:45], 0
	v_mov_b64_e32 v[46:47], 0
	v_mov_b64_e32 v[48:49], 0
	v_mov_b64_e32 v[50:51], 0
	v_mov_b64_e32 v[52:53], 0
	v_mov_b64_e32 v[54:55], 0
	v_mov_b64_e32 v[56:57], 0
	v_mov_b64_e32 v[58:59], 0
	v_mov_b64_e32 v[60:61], 0
	v_mov_b64_e32 v[62:63], 0
	v_mov_b64_e32 v[64:65], 0
	v_mov_b64_e32 v[66:67], 0
	v_mov_b64_e32 v[68:69], 0
	v_mov_b64_e32 v[70:71], 0
	v_mov_b64_e32 v[72:73], 0
	v_mov_b64_e32 v[74:75], 0
	v_mov_b64_e32 v[76:77], 0
	v_mov_b64_e32 v[78:79], 0
	v_mov_b64_e32 v[80:81], 0
	v_mov_b64_e32 v[82:83], 0
	v_mov_b64_e32 v[84:85], 0
	v_mov_b64_e32 v[86:87], 0
	v_mov_b64_e32 v[88:89], 0
	v_mov_b64_e32 v[90:91], 0
	v_mov_b64_e32 v[92:93], 0
	v_mov_b64_e32 v[94:95], 0
	v_mov_b64_e32 v[96:97], 0
	v_mov_b64_e32 v[98:99], 0
	v_mov_b64_e32 v[100:101], 0
	v_mov_b64_e32 v[102:103], 0
	v_mov_b64_e32 v[104:105], 0
	v_mov_b64_e32 v[106:107], 0
	v_mov_b64_e32 v[108:109], 0
	v_mov_b64_e32 v[110:111], 0
	v_mov_b64_e32 v[112:113], 0
	v_mov_b64_e32 v[114:115], 0
	v_mov_b64_e32 v[116:117], 0
	v_mov_b64_e32 v[118:119], 0
	v_mov_b64_e32 v[120:121], 0
	v_mov_b64_e32 v[122:123], 0
	v_mov_b64_e32 v[124:125], 0
	v_mov_b64_e32 v[126:127], 0
	v_mov_b64_e32 v[128:129], 0

; template <class Epi, class Sched, bool ALIGN_EPI = false, bool SP2 = false, bool F8 = false>
; __device__ __forceinline__ void gemm_phase(PG8_LAS unsigned char* lds, const Gemm g, const Sched& S, const Epi& E) {
;     ...
;         const bool has_next = S.next(ui + 1, nxt);
;         const char* nA = has_next ? (const char*)g.A + (size_t)nxt.pm * tstep + nxt.ko : cA; const char* nB = has_next ? (const char*)g.Bt + (size_t)nxt.pn * tstep + nxt.ko : cB;
;     ...
; #pragma unroll
;         for (int a = 0; a < 2; ++a)
; #pragma unroll
;             for (int b = 0; b < 2; ++b)
; #pragma unroll
;                 for (int m = 0; m < 4; ++m)
; #pragma unroll
;                     for (int n = 0; n < 2; ++n) acc[a][b][m][n] = (f32x4){0.f, 0.f, 0.f, 0.f};
;         cur = nxt; cA = nA; cB = nB; ++ui;
.LBB0_801:
	s_ashr_i32 s25, s24, 31
	s_lshl_b64 s[4:5], s[24:25], 18
	s_add_u32 s36, s49, s4
	s_addc_u32 s37, s50, s5
	s_and_b64 s[4:5], s[8:9], exec
	s_cselect_b32 s25, s37, s43
	s_cselect_b32 s83, s36, s42
	s_ashr_i32 s31, s30, 31
	s_lshl_b64 s[4:5], s[30:31], 18
	s_add_u32 s38, s51, s4
	s_addc_u32 s39, s52, s5
	s_and_b64 s[4:5], s[8:9], exec
	s_cselect_b32 s31, s39, s45
	s_cselect_b32 s84, s38, s44
	s_add_u32 s42, s42, 0x20080
	s_addc_u32 s43, s43, 0
	s_add_u32 s85, s44, 0x100
	v_mov_b32_e32 v34, 0
	s_addc_u32 s86, s45, 0
	s_mov_b32 s87, -2
	v_mov_b32_e32 v35, 0
	v_mov_b64_e32 v[36:37], 0
	v_mov_b64_e32 v[38:39], 0
	v_mov_b64_e32 v[40:41], 0
	v_mov_b64_e32 v[42:43], 0
	v_mov_b64_e32 v[44:45], 0
	v_mov_b64_e32 v[46:47], 0
	v_mov_b64_e32 v[48:49], 0
	v_mov_b64_e32 v[50:51], 0
	v_mov_b64_e32 v[52:53], 0
	v_mov_b64_e32 v[54:55], 0
	v_mov_b64_e32 v[56:57], 0
	v_mov_b64_e32 v[58:59], 0
	v_mov_b64_e32 v[60:61], 0
	v_mov_b64_e32 v[62:63], 0
	v_mov_b64_e32 v[64:65], 0
	v_mov_b64_e32 v[66:67], 0
	v_mov_b64_e32 v[68:69], 0
	v_mov_b64_e32 v[70:71], 0
	v_mov_b64_e32 v[72:73], 0
	v_mov_b64_e32 v[74:75], 0
	v_mov_b64_e32 v[76:77], 0
	v_mov_b64_e32 v[78:79], 0
	v_mov_b64_e32 v[80:81], 0
	v_mov_b64_e32 v[82:83], 0
	v_mov_b64_e32 v[84:85], 0
	v_mov_b64_e32 v[86:87], 0
	v_mov_b64_e32 v[88:89], 0
	v_mov_b64_e32 v[90:91], 0
	v_mov_b64_e32 v[92:93], 0
	v_mov_b64_e32 v[94:95], 0
	v_mov_b64_e32 v[96:97], 0
	v_mov_b64_e32 v[98:99], 0
	v_mov_b64_e32 v[100:101], 0
	v_mov_b64_e32 v[102:103], 0
	v_mov_b64_e32 v[104:105], 0
	v_mov_b64_e32 v[106:107], 0
	v_mov_b64_e32 v[108:109], 0
	v_mov_b64_e32 v[110:111], 0
	v_mov_b64_e32 v[112:113], 0
	v_mov_b64_e32 v[114:115], 0
	v_mov_b64_e32 v[116:117], 0
	v_mov_b64_e32 v[118:119], 0
	v_mov_b64_e32 v[120:121], 0
	v_mov_b64_e32 v[122:123], 0
	v_mov_b64_e32 v[124:125], 0
	v_mov_b64_e32 v[126:127], 0
	v_mov_b64_e32 v[128:129], 0
	v_mov_b64_e32 v[130:131], 0
	v_mov_b64_e32 v[132:133], 0
	v_mov_b64_e32 v[134:135], 0
	v_mov_b64_e32 v[136:137], 0
	v_mov_b64_e32 v[138:139], 0
	v_mov_b64_e32 v[140:141], 0
	v_mov_b64_e32 v[142:143], 0
	v_mov_b64_e32 v[144:145], 0
	v_mov_b64_e32 v[146:147], 0
	v_mov_b64_e32 v[148:149], 0
	v_mov_b64_e32 v[150:151], 0
	v_mov_b64_e32 v[152:153], 0
	v_mov_b64_e32 v[154:155], 0
	v_mov_b64_e32 v[156:157], 0
	v_mov_b64_e32 v[158:159], 0
	v_mov_b64_e32 v[160:161], 0

; template <class Epi, class Sched, bool ALIGN_EPI = false, bool SP2 = false, bool F8 = false>
; __device__ __forceinline__ void gemm_phase(PG8_LAS unsigned char* lds, const Gemm g, const Sched& S, const Epi& E) {
;     ...
;         const bool has_next = S.next(ui + 1, nxt);
;         const char* nA = has_next ? (const char*)g.A + (size_t)nxt.pm * tstep + nxt.ko : cA; const char* nB = has_next ? (const char*)g.Bt + (size_t)nxt.pn * tstep + nxt.ko : cB;
;     ...
; #pragma unroll
;         for (int a = 0; a < 2; ++a)
; #pragma unroll
;             for (int b = 0; b < 2; ++b)
; #pragma unroll
;                 for (int m = 0; m < 4; ++m)
; #pragma unroll
;                     for (int n = 0; n < 2; ++n) acc[a][b][m][n] = (f32x4){0.f, 0.f, 0.f, 0.f};
;         cur = nxt; cA = nA; cB = nB; ++ui;
.LBB0_1309:
	s_ashr_i32 s25, s24, 31
	s_lshl_b64 s[4:5], s[24:25], 18
	s_add_u32 s30, s48, s4
	s_addc_u32 s31, s49, s5
	s_and_b64 s[4:5], s[22:23], exec
	s_cselect_b32 s25, s31, s43
	s_cselect_b32 s77, s30, s42
	s_ashr_i32 s27, s26, 31
	s_lshl_b64 s[4:5], s[26:27], 18
	s_add_u32 s36, s50, s4
	s_addc_u32 s37, s51, s5
	s_and_b64 s[4:5], s[22:23], exec
	s_cselect_b32 s27, s37, s45
	s_cselect_b32 s78, s36, s44
	s_add_u32 s42, s42, 0x20080
	s_addc_u32 s43, s43, 0
	s_add_u32 s79, s44, 0x100
	v_mov_b32_e32 v34, 0
	s_addc_u32 s80, s45, 0
	s_mov_b32 s81, -2
	v_mov_b32_e32 v35, 0
	v_mov_b64_e32 v[36:37], 0
	v_mov_b64_e32 v[38:39], 0
	v_mov_b64_e32 v[40:41], 0
	v_mov_b64_e32 v[42:43], 0
	v_mov_b64_e32 v[44:45], 0
	v_mov_b64_e32 v[46:47], 0
	v_mov_b64_e32 v[48:49], 0
	v_mov_b64_e32 v[50:51], 0
	v_mov_b64_e32 v[52:53], 0
	v_mov_b64_e32 v[54:55], 0
	v_mov_b64_e32 v[56:57], 0
	v_mov_b64_e32 v[58:59], 0
	v_mov_b64_e32 v[60:61], 0
	v_mov_b64_e32 v[62:63], 0
	v_mov_b64_e32 v[64:65], 0
	v_mov_b64_e32 v[66:67], 0
	v_mov_b64_e32 v[68:69], 0
	v_mov_b64_e32 v[70:71], 0
	v_mov_b64_e32 v[72:73], 0
	v_mov_b64_e32 v[74:75], 0
	v_mov_b64_e32 v[76:77], 0
	v_mov_b64_e32 v[78:79], 0
	v_mov_b64_e32 v[80:81], 0
	v_mov_b64_e32 v[82:83], 0
	v_mov_b64_e32 v[84:85], 0
	v_mov_b64_e32 v[86:87], 0
	v_mov_b64_e32 v[88:89], 0
	v_mov_b64_e32 v[90:91], 0
	v_mov_b64_e32 v[92:93], 0
	v_mov_b64_e32 v[94:95], 0
	v_mov_b64_e32 v[96:97], 0
	v_mov_b64_e32 v[98:99], 0
	v_mov_b64_e32 v[100:101], 0
	v_mov_b64_e32 v[102:103], 0
	v_mov_b64_e32 v[104:105], 0
	v_mov_b64_e32 v[106:107], 0
	v_mov_b64_e32 v[108:109], 0
	v_mov_b64_e32 v[110:111], 0
	v_mov_b64_e32 v[112:113], 0
	v_mov_b64_e32 v[114:115], 0
	v_mov_b64_e32 v[116:117], 0
	v_mov_b64_e32 v[118:119], 0
	v_mov_b64_e32 v[120:121], 0
	v_mov_b64_e32 v[122:123], 0
	v_mov_b64_e32 v[124:125], 0
	v_mov_b64_e32 v[126:127], 0
	v_mov_b64_e32 v[128:129], 0
	v_mov_b64_e32 v[130:131], 0
	v_mov_b64_e32 v[132:133], 0
	v_mov_b64_e32 v[134:135], 0
	v_mov_b64_e32 v[136:137], 0
	v_mov_b64_e32 v[138:139], 0
	v_mov_b64_e32 v[140:141], 0
	v_mov_b64_e32 v[142:143], 0
	v_mov_b64_e32 v[144:145], 0
	v_mov_b64_e32 v[146:147], 0
	v_mov_b64_e32 v[148:149], 0
	v_mov_b64_e32 v[150:151], 0
	v_mov_b64_e32 v[152:153], 0
	v_mov_b64_e32 v[154:155], 0
	v_mov_b64_e32 v[156:157], 0
	v_mov_b64_e32 v[158:159], 0
	v_mov_b64_e32 v[160:161], 0

; template <class Epi, class Sched, bool ALIGN_EPI = false, bool SP2 = false, bool F8 = false>
; __device__ __forceinline__ void gemm_phase(PG8_LAS unsigned char* lds, const Gemm g, const Sched& S, const Epi& E) {
;     ...
;         const char* nA = has_next ? (const char*)g.A + (size_t)nxt.pm * tstep + nxt.ko : cA; const char* nB = has_next ? (const char*)g.Bt + (size_t)nxt.pn * tstep + nxt.ko : cB;
;     ...
; #pragma unroll
;         for (int a = 0; a < 2; ++a)
; #pragma unroll
;             for (int b = 0; b < 2; ++b)
; #pragma unroll
;                 for (int m = 0; m < 4; ++m)
; #pragma unroll
;                     for (int n = 0; n < 2; ++n) acc[a][b][m][n] = (f32x4){0.f, 0.f, 0.f, 0.f};
;         cur = nxt; cA = nA; cB = nB; ++ui;
.LBB0_1391:
	v_mov_b32_e32 v34, 0
	v_lshl_add_u64 v[180:181], v[2:3], 0, s[24:25]
	s_mov_b32 s76, -2
	v_mov_b32_e32 v35, 0
	v_mov_b64_e32 v[36:37], 0
	v_mov_b64_e32 v[38:39], 0
	v_mov_b64_e32 v[40:41], 0
	v_mov_b64_e32 v[42:43], 0
	v_mov_b64_e32 v[44:45], 0
	v_mov_b64_e32 v[46:47], 0
	v_mov_b64_e32 v[48:49], 0
	v_mov_b64_e32 v[50:51], 0
	v_mov_b64_e32 v[52:53], 0
	v_mov_b64_e32 v[54:55], 0
	v_mov_b64_e32 v[56:57], 0
	v_mov_b64_e32 v[58:59], 0
	v_mov_b64_e32 v[60:61], 0
	v_mov_b64_e32 v[62:63], 0
	v_mov_b64_e32 v[64:65], 0
	v_mov_b64_e32 v[66:67], 0
	v_mov_b64_e32 v[68:69], 0
	v_mov_b64_e32 v[70:71], 0
	v_mov_b64_e32 v[72:73], 0
	v_mov_b64_e32 v[74:75], 0
	v_mov_b64_e32 v[76:77], 0
	v_mov_b64_e32 v[78:79], 0
	v_mov_b64_e32 v[80:81], 0
	v_mov_b64_e32 v[82:83], 0
	v_mov_b64_e32 v[84:85], 0
	v_mov_b64_e32 v[86:87], 0
	v_mov_b64_e32 v[88:89], 0
	v_mov_b64_e32 v[90:91], 0
	v_mov_b64_e32 v[92:93], 0
	v_mov_b64_e32 v[94:95], 0
	v_mov_b64_e32 v[96:97], 0
	v_mov_b64_e32 v[98:99], 0
	v_mov_b64_e32 v[100:101], 0
	v_mov_b64_e32 v[102:103], 0
	v_mov_b64_e32 v[104:105], 0
	v_mov_b64_e32 v[106:107], 0
	v_mov_b64_e32 v[108:109], 0
	v_mov_b64_e32 v[110:111], 0
	v_mov_b64_e32 v[112:113], 0
	v_mov_b64_e32 v[114:115], 0
	v_mov_b64_e32 v[116:117], 0
	v_mov_b64_e32 v[118:119], 0
	v_mov_b64_e32 v[120:121], 0
	v_mov_b64_e32 v[122:123], 0
	v_mov_b64_e32 v[124:125], 0
	v_mov_b64_e32 v[126:127], 0
	v_mov_b64_e32 v[128:129], 0
	v_mov_b64_e32 v[130:131], 0
	v_mov_b64_e32 v[132:133], 0
	v_mov_b64_e32 v[134:135], 0
	v_mov_b64_e32 v[136:137], 0
	v_mov_b64_e32 v[138:139], 0
	v_mov_b64_e32 v[140:141], 0
	v_mov_b64_e32 v[142:143], 0
	v_mov_b64_e32 v[144:145], 0
	v_mov_b64_e32 v[146:147], 0
	v_mov_b64_e32 v[148:149], 0
	v_mov_b64_e32 v[150:151], 0
	v_mov_b64_e32 v[152:153], 0
	v_mov_b64_e32 v[154:155], 0
	v_mov_b64_e32 v[156:157], 0
	v_mov_b64_e32 v[158:159], 0
	v_mov_b64_e32 v[160:161], 0
